# combined: P2 two-deep prefetch + counted waits at GEMM unit starts (P1,P5,P8) and at P11's second epilogue wait, on top of hosted/pipelined conversion + nt loads
# baseline (speedup 1.0000x reference)
; #define EPI_FENCE() asm volatile("" ::: "memory")
;     __device__ __forceinline__ void operator()(const f32x4 (&acc)[2][2][4][2], const Unit& u, int wr, int wc, int fr, int fq) const {
;     ...
;             u32x4 pb[8][2];
;     ...
;             EPIRES_LD(0); EPIRES_LD(1); EPIRES_LD(2); EPIRES_LD(3); EPIRES_LD(4); EPIRES_LD(5);
;             EPI_FENCE();
.LBB0_1425:
	s_lshl_b32 s13, s48, 8
	s_lshl_b32 s12, s49, 8
	s_add_i32 s13, s13, s30
	s_or_b32 s12, s12, s31
	v_or_b32_e32 v198, s13, v187
	s_ashr_i32 s13, s13, 2
	s_andn2_b32 s13, s13, 63
	s_ashr_i32 s15, s12, 6
	s_add_i32 s16, s13, s15
	s_ashr_i32 s17, s16, 31
	s_lshl_b64 s[16:17], s[16:17], 15
	s_add_u32 s18, s82, s16
	v_lshlrev_b32_e32 v128, 6, v198
	s_addc_u32 s19, s83, s17
	s_or_b32 s14, s15, 2
	v_and_b32_e32 v128, 0x3c0, v128
	v_lshlrev_b32_e32 v131, 2, v198
	s_add_i32 s48, s13, s14
	v_and_b32_e32 v131, 32, v131
	v_or_b32_e32 v143, v128, v193
	s_ashr_i32 s49, s48, 31
	v_bitop3_b32 v138, v143, s42, v131 bitop3:0xde
	s_lshl_b64 s[48:49], s[48:49], 15
	v_or3_b32 v142, v191, v128, v131
	v_bitop3_b32 v134, s16, -2, v138 bitop3:0xc8
	v_mov_b32_e32 v135, s17
	s_add_u32 s50, s82, s48
	v_bitop3_b32 v138, s48, -2, v138 bitop3:0xc8
	v_mov_b32_e32 v139, s49
	v_lshl_add_u64 v[136:137], s[82:83], 0, v[134:135]
	s_addc_u32 s51, s83, s49
	v_lshl_add_u64 v[140:141], s[82:83], 0, v[138:139]
	global_load_dwordx2 v[200:201], v142, s[18:19]
	global_load_dwordx2 v[202:203], v[136:137], off
	global_load_dwordx2 v[204:205], v[140:141], off
	global_load_dwordx2 v[206:207], v142, s[50:51]
	v_or_b32_e32 v182, 16, v198
	v_lshrrev_b32_e32 v134, 3, v182
	v_and_or_b32 v134, v134, 10, s29
	v_lshlrev_b32_e32 v134, 10, v134
	v_or3_b32 v128, v128, v192, v131
	v_bitop3_b32 v131, v143, s39, v131 bitop3:0xde
	v_or_b32_e32 v138, v131, v134
	v_or_b32_e32 v142, v128, v134
	v_bitop3_b32 v134, s16, -2, v138 bitop3:0xc8
	v_bitop3_b32 v138, s48, -2, v138 bitop3:0xc8
	v_lshl_add_u64 v[136:137], s[82:83], 0, v[134:135]
	v_lshl_add_u64 v[140:141], s[82:83], 0, v[138:139]
	global_load_dwordx2 v[208:209], v142, s[18:19]
	global_load_dwordx2 v[184:185], v[136:137], off
	global_load_dwordx2 v[178:179], v[140:141], off
	global_load_dwordx2 v[180:181], v142, s[50:51]
	v_or_b32_e32 v172, 32, v198
	v_lshrrev_b32_e32 v134, 3, v172
	v_and_or_b32 v134, v134, 12, s40
	v_lshlrev_b32_e32 v134, 10, v134
	v_or_b32_e32 v138, v131, v134
	v_or_b32_e32 v142, v128, v134
	v_bitop3_b32 v134, s16, -2, v138 bitop3:0xc8
	v_or_b32_e32 v162, 48, v198
	v_lshl_add_u64 v[136:137], s[82:83], 0, v[134:135]
	v_lshrrev_b32_e32 v134, 3, v162
	v_and_or_b32 v134, v134, 14, s29
	v_lshlrev_b32_e32 v134, 10, v134
	v_bitop3_b32 v138, s48, -2, v138 bitop3:0xc8
	v_or_b32_e32 v131, v131, v134
	v_lshl_add_u64 v[140:141], s[82:83], 0, v[138:139]
	v_or_b32_e32 v128, v128, v134
	v_bitop3_b32 v134, s16, -2, v131 bitop3:0xc8
	v_bitop3_b32 v138, s48, -2, v131 bitop3:0xc8
	v_add_u32_e32 v146, 0x80, v198
	global_load_dwordx2 v[176:177], v142, s[18:19]
	global_load_dwordx2 v[174:175], v[136:137], off
	global_load_dwordx2 v[168:169], v[140:141], off
	global_load_dwordx2 v[170:171], v142, s[50:51]
	v_lshl_add_u64 v[134:135], s[82:83], 0, v[134:135]
	v_lshl_add_u64 v[136:137], s[82:83], 0, v[138:139]
	global_load_dwordx2 v[166:167], v128, s[18:19]
	global_load_dwordx2 v[164:165], v[134:135], off
	global_load_dwordx2 v[154:155], v[136:137], off
	global_load_dwordx2 v[158:159], v128, s[50:51]
	v_ashrrev_i32_e32 v128, 2, v146
	v_and_b32_e32 v131, 0xffffffc0, v128
	v_lshlrev_b32_e32 v128, 7, v146
	v_and_b32_e32 v138, 0x4000, v128
	v_lshlrev_b32_e32 v128, 6, v146
	v_and_b32_e32 v139, 0x3c0, v128
	v_lshlrev_b32_e32 v128, 2, v146
	v_and_b32_e32 v140, 32, v128
	v_or_b32_e32 v128, v139, v190
	v_bitop3_b32 v139, v139, v140, v193 bitop3:0x36
	v_add_u32_e32 v134, s15, v131
	v_or3_b32 v128, v128, v138, v140
	v_or3_b32 v142, s41, v139, v138
	v_add_u32_e32 v138, s14, v131
	v_ashrrev_i32_e32 v135, 31, v134
	v_ashrrev_i32_e32 v139, 31, v138
	v_lshlrev_b64 v[134:135], 15, v[134:135]
	v_lshlrev_b64 v[138:139], 15, v[138:139]
	v_lshl_add_u64 v[136:137], s[82:83], 0, v[134:135]
	v_lshl_add_u64 v[140:141], s[82:83], 0, v[138:139]
	v_lshl_add_u64 v[136:137], v[136:137], 0, v[128:129]
	v_bitop3_b32 v134, v134, -2, v142 bitop3:0xc8
	v_lshl_add_u64 v[140:141], v[140:141], 0, v[128:129]
	v_bitop3_b32 v138, v138, -2, v142 bitop3:0xc8
	v_lshl_add_u64 v[134:135], s[82:83], 0, v[134:135]
	v_lshl_add_u64 v[138:139], s[82:83], 0, v[138:139]
	global_load_dwordx2 v[160:161], v[136:137], off
	global_load_dwordx2 v[156:157], v[134:135], off
	global_load_dwordx2 v[148:149], v[140:141], off
	global_load_dwordx2 v[144:145], v[138:139], off
	v_add_u32_e32 v140, 0x90, v198
	v_ashrrev_i32_e32 v128, 2, v140
	v_and_b32_e32 v131, 0xffffffc0, v128
	v_lshlrev_b32_e32 v128, 7, v140
	v_and_b32_e32 v138, 0x4000, v128
	v_lshrrev_b32_e32 v128, 3, v140
	v_and_or_b32 v128, v128, 10, s40
	v_lshlrev_b32_e32 v136, 6, v140
	v_lshlrev_b32_e32 v139, 2, v140
	v_lshlrev_b32_e32 v141, 10, v128
	v_and_b32_e32 v137, 32, v139
	v_and_or_b32 v142, v136, s38, v188
	v_or_b32_e32 v128, v141, v138
	v_add_u32_e32 v134, s15, v131
	v_or3_b32 v128, v128, v142, v137
	v_bitop3_b32 v139, v142, v139, 32 bitop3:0x72
	v_add_u32_e32 v142, s14, v131
	v_ashrrev_i32_e32 v135, 31, v134
	v_ashrrev_i32_e32 v143, 31, v142
	v_lshlrev_b64 v[134:135], 15, v[134:135]
	v_or3_b32 v138, v138, v139, v141
	v_mov_b32_e32 v139, v129
	v_lshlrev_b64 v[142:143], 15, v[142:143]
	v_lshl_add_u64 v[136:137], s[82:83], 0, v[134:135]
	v_lshl_add_u64 v[134:135], v[134:135], 0, v[138:139]
	v_lshl_add_u64 v[138:139], v[142:143], 0, v[138:139]
	v_and_b32_e32 v134, -2, v134
	v_and_b32_e32 v138, -2, v138
	v_lshl_add_u64 v[136:137], v[136:137], 0, v[128:129]
	v_lshl_add_u64 v[134:135], s[82:83], 0, v[134:135]
	v_lshl_add_u64 v[150:151], s[82:83], 0, v[142:143]
	v_lshl_add_u64 v[138:139], s[82:83], 0, v[138:139]
	v_lshl_add_u64 v[210:211], v[150:151], 0, v[128:129]
	global_load_dwordx2 v[152:153], v[136:137], off
	global_load_dwordx2 v[150:151], v[134:135], off
	global_load_dwordx2 v[142:143], v[210:211], off
	s_nop 0
	global_load_dwordx2 v[138:139], v[138:139], off
	v_add_u32_e32 v134, 0xb0, v198
	v_ashrrev_i32_e32 v199, 31, v198
	v_add_u32_e32 v136, 0xa0, v198
	v_ashrrev_i32_e32 v131, 2, v134
	s_ashr_i32 s13, s12, 31
	v_lshlrev_b64 v[198:199], 14, v[198:199]
	v_and_b32_e32 v173, 0xffffffc0, v131
	v_lshlrev_b32_e32 v131, 7, v134
	s_waitcnt vmcnt(0)
; __device__ __forceinline__ unsigned pk_bf16(float lo, float hi) { const f32x2 f = {lo, hi}; const bf16v2 r = __builtin_convertvector(f, bf16v2); return __builtin_bit_cast(unsigned, r); }
; __device__ __forceinline__ float dot4(const f32x4 a, const f32x4 b) { return (a[0] * b[0] + a[1] * b[1]) + (a[2] * b[2] + a[3] * b[3]); }
; #define EPI_FENCE() asm volatile("" ::: "memory")
; __device__ __forceinline__ f32x4 bf4_lo(const u32x4 w) { return (f32x4){__builtin_bit_cast(float, w.x << 16), __builtin_bit_cast(float, w.x & 0xffff0000u), __builtin_bit_cast(float, w.y << 16), __builtin_bit_cast(float, w.y & 0xffff0000u)}; }
; __device__ __forceinline__ f32x4 bf4_hi(const u32x4 w) { return (f32x4){__builtin_bit_cast(float, w.z << 16), __builtin_bit_cast(float, w.z & 0xffff0000u), __builtin_bit_cast(float, w.w << 16), __builtin_bit_cast(float, w.w & 0xffff0000u)}; }
;     __device__ __forceinline__ void operator()(const f32x4 (&acc)[2][2][4][2], const Unit& u, int wr, int wc, int fr, int fq) const {
;     ...
;             for (int g = 0; g < 8; ++g) {
;                 const int ai = g >> 2, m = g & 3, row = rowb + ai * HALF + m * 16; float s = 0.f;
;                 if (g == 2) { EPIRES_LD(6); EPIRES_LD(7); EPI_FENCE(); }
; #pragma unroll
;                 for (int bj = 0; bj < 2; ++bj) {
;                     const f32x4 o0 = bf4_lo(pb[g][bj]) + acc[ai][bj][m][0], o1 = bf4_hi(pb[g][bj]) + acc[ai][bj][m][1];
;                     if (MODE == 2) { float* p = out + (size_t)row * 4096 + colb + 4 * fq + bj * HALF; *(f32x4*)p = o0; *(f32x4*)(p + 16) = o1; }
;                     else { u32x4 w; w.x = pk_bf16(o0[0], o0[1]); w.y = pk_bf16(o0[2], o0[3]); w.z = pk_bf16(o1[0], o1[1]); w.w = pk_bf16(o1[2], o1[3]); *(u32x4*)(hb + blk_elem(row, colb + 8 * fq + bj * HALF, 4096)) = w; s += dot4(o0, o0) + dot4(o1, o1); }
	v_lshlrev_b32_e32 v210, 16, v200
	v_and_b32_e32 v211, 0xffff0000, v200
	v_lshlrev_b32_e32 v200, 16, v201
	v_and_b32_e32 v201, 0xffff0000, v201
	v_lshl_add_u64 v[198:199], s[78:79], 0, v[198:199]
	s_lshl_b64 s[12:13], s[12:13], 2
	v_and_b32_e32 v212, 0x4000, v131
	v_pk_add_f32 v[126:127], v[126:127], v[200:201]
	v_lshlrev_b32_e32 v200, 16, v202
	v_and_b32_e32 v201, 0xffff0000, v202
	v_lshl_add_u64 v[198:199], v[198:199], 0, s[12:13]
	v_mov_b32_e32 v131, v129
	v_pk_add_f32 v[124:125], v[124:125], v[210:211]
	v_lshlrev_b32_e32 v202, 16, v203
	v_and_b32_e32 v203, 0xffff0000, v203
	v_pk_add_f32 v[120:121], v[120:121], v[200:201]
	v_lshl_add_u64 v[198:199], v[198:199], 0, v[130:131]
	v_pk_add_f32 v[122:123], v[122:123], v[202:203]
	global_store_dwordx4 v[198:199], v[124:127], off
	global_store_dwordx4 v[198:199], v[120:123], off offset:64
	v_ashrrev_i32_e32 v183, 31, v182
	v_ashrrev_i32_e32 v128, 2, v136
	v_lshlrev_b32_e32 v120, 16, v206
	v_and_b32_e32 v121, 0xffff0000, v206
	v_lshlrev_b32_e32 v122, 16, v207
	v_and_b32_e32 v123, 0xffff0000, v207
	v_pk_add_f32 v[116:117], v[116:117], v[120:121]
	v_lshlrev_b32_e32 v120, 16, v204
	v_and_b32_e32 v121, 0xffff0000, v204
	v_pk_add_f32 v[118:119], v[118:119], v[122:123]
	v_lshlrev_b32_e32 v122, 16, v205
	v_and_b32_e32 v123, 0xffff0000, v205
	v_pk_add_f32 v[108:109], v[108:109], v[120:121]
	v_pk_add_f32 v[110:111], v[110:111], v[122:123]
	global_store_dwordx4 v[198:199], v[116:119], off offset:512
	global_store_dwordx4 v[198:199], v[108:111], off offset:576
	v_and_b32_e32 v135, 0xffffffc0, v128
	v_lshlrev_b64 v[116:117], 14, v[182:183]
	v_lshlrev_b32_e32 v108, 16, v208
	v_and_b32_e32 v109, 0xffff0000, v208
	v_pk_add_f32 v[108:109], v[112:113], v[108:109]
	v_lshlrev_b32_e32 v112, 16, v184
	v_and_b32_e32 v113, 0xffff0000, v184
	v_lshlrev_b32_e32 v110, 16, v209
	v_and_b32_e32 v111, 0xffff0000, v209
	v_pk_add_f32 v[104:105], v[104:105], v[112:113]
	v_lshl_add_u64 v[112:113], s[78:79], 0, v[116:117]
	v_pk_add_f32 v[110:111], v[114:115], v[110:111]
	v_lshlrev_b32_e32 v114, 16, v185
	v_and_b32_e32 v115, 0xffff0000, v185
	v_lshl_add_u64 v[112:113], v[112:113], 0, s[12:13]
	v_pk_add_f32 v[106:107], v[106:107], v[114:115]
	v_lshl_add_u64 v[112:113], v[112:113], 0, v[130:131]
	global_store_dwordx4 v[112:113], v[108:111], off
	global_store_dwordx4 v[112:113], v[104:107], off offset:64
	v_lshlrev_b32_e32 v128, 7, v136
	v_and_b32_e32 v137, 0x4000, v128
	v_lshlrev_b32_e32 v106, 16, v181
	v_and_b32_e32 v107, 0xffff0000, v181
	v_lshlrev_b32_e32 v104, 16, v180
	v_and_b32_e32 v105, 0xffff0000, v180
	v_pk_add_f32 v[102:103], v[102:103], v[106:107]
	v_lshlrev_b32_e32 v106, 16, v179
	v_and_b32_e32 v107, 0xffff0000, v179
	v_lshrrev_b32_e32 v128, 3, v136
	v_pk_add_f32 v[100:101], v[100:101], v[104:105]
	v_lshlrev_b32_e32 v104, 16, v178
	v_and_b32_e32 v105, 0xffff0000, v178
	v_pk_add_f32 v[98:99], v[98:99], v[106:107]
	v_pk_add_f32 v[96:97], v[96:97], v[104:105]
	global_store_dwordx4 v[112:113], v[100:103], off offset:512
	global_store_dwordx4 v[112:113], v[96:99], off offset:576
	v_lshlrev_b32_e32 v141, 6, v136
	v_lshlrev_b32_e32 v147, 2, v136
	v_and_or_b32 v98, v128, 12, s40
	v_lshlrev_b32_e32 v100, 10, v98
	v_and_b32_e32 v163, 32, v147
	v_add_u32_e32 v96, s15, v135
	v_and_or_b32 v101, v141, s38, v188
	v_or_b32_e32 v98, v100, v137
	v_add_u32_e32 v102, s14, v135
	v_ashrrev_i32_e32 v97, 31, v96
	v_or3_b32 v128, v98, v101, v163
	v_bitop3_b32 v101, v101, v147, 32 bitop3:0x72
	v_ashrrev_i32_e32 v103, 31, v102
	v_lshlrev_b64 v[96:97], 15, v[96:97]
	v_or3_b32 v100, v137, v101, v100
	v_mov_b32_e32 v101, v129
	v_lshlrev_b64 v[102:103], 15, v[102:103]
	v_lshl_add_u64 v[98:99], s[82:83], 0, v[96:97]
	v_lshl_add_u64 v[96:97], v[96:97], 0, v[100:101]
	v_lshl_add_u64 v[100:101], v[102:103], 0, v[100:101]
	v_lshl_add_u64 v[104:105], s[82:83], 0, v[102:103]
	v_and_b32_e32 v100, -2, v100
	v_lshrrev_b32_e32 v213, 3, v134
	v_lshl_add_u64 v[98:99], v[98:99], 0, v[128:129]
	v_and_b32_e32 v96, -2, v96
	v_lshl_add_u64 v[104:105], v[104:105], 0, v[128:129]
	v_lshl_add_u64 v[100:101], s[82:83], 0, v[100:101]
	v_lshl_add_u64 v[96:97], s[82:83], 0, v[96:97]
	global_load_dwordx2 v[110:111], v[98:99], off
	global_load_dwordx2 v[108:109], v[96:97], off
	s_nop 0
	global_load_dwordx2 v[104:105], v[104:105], off
	s_nop 0
	global_load_dwordx2 v[100:101], v[100:101], off
	v_and_or_b32 v98, v213, 14, s40
	v_lshlrev_b32_e32 v214, 6, v134
	v_lshlrev_b32_e32 v215, 2, v134
	v_lshlrev_b32_e32 v102, 10, v98
	v_and_b32_e32 v216, 32, v215
	v_add_u32_e32 v96, s15, v173
	v_and_or_b32 v103, v214, s38, v188
	v_or_b32_e32 v98, v102, v212
	v_ashrrev_i32_e32 v97, 31, v96
	v_or3_b32 v128, v98, v103, v216
	v_bitop3_b32 v103, v103, v215, 32 bitop3:0x72
	v_add_u32_e32 v106, s14, v173
	v_lshlrev_b64 v[96:97], 15, v[96:97]
	v_or3_b32 v102, v212, v103, v102
	v_mov_b32_e32 v103, v129
	v_ashrrev_i32_e32 v107, 31, v106
	v_lshl_add_u64 v[98:99], s[82:83], 0, v[96:97]
	v_lshl_add_u64 v[96:97], v[96:97], 0, v[102:103]
	v_lshlrev_b64 v[106:107], 15, v[106:107]
	v_and_b32_e32 v96, -2, v96
	v_lshl_add_u64 v[102:103], v[106:107], 0, v[102:103]
	v_lshl_add_u64 v[98:99], v[98:99], 0, v[128:129]
	v_lshl_add_u64 v[96:97], s[82:83], 0, v[96:97]
	v_lshl_add_u64 v[112:113], s[82:83], 0, v[106:107]
	v_and_b32_e32 v102, -2, v102
	v_lshl_add_u64 v[112:113], v[112:113], 0, v[128:129]
	v_lshl_add_u64 v[114:115], s[82:83], 0, v[102:103]
	global_load_dwordx2 v[106:107], v[98:99], off
	global_load_dwordx2 v[102:103], v[96:97], off
	s_nop 0
	global_load_dwordx2 v[98:99], v[112:113], off
	global_load_dwordx2 v[96:97], v[114:115], off
	v_ashrrev_i32_e32 v173, 31, v172
	v_lshlrev_b64 v[112:113], 14, v[172:173]
; __device__ __forceinline__ unsigned pk_bf16(float lo, float hi) { const f32x2 f = {lo, hi}; const bf16v2 r = __builtin_convertvector(f, bf16v2); return __builtin_bit_cast(unsigned, r); }
; __device__ __forceinline__ float dot4(const f32x4 a, const f32x4 b) { return (a[0] * b[0] + a[1] * b[1]) + (a[2] * b[2] + a[3] * b[3]); }
; #define EPI_FENCE() asm volatile("" ::: "memory")
; __device__ __forceinline__ f32x4 bf4_lo(const u32x4 w) { return (f32x4){__builtin_bit_cast(float, w.x << 16), __builtin_bit_cast(float, w.x & 0xffff0000u), __builtin_bit_cast(float, w.y << 16), __builtin_bit_cast(float, w.y & 0xffff0000u)}; }
; __device__ __forceinline__ f32x4 bf4_hi(const u32x4 w) { return (f32x4){__builtin_bit_cast(float, w.z << 16), __builtin_bit_cast(float, w.z & 0xffff0000u), __builtin_bit_cast(float, w.w << 16), __builtin_bit_cast(float, w.w & 0xffff0000u)}; }
;     __device__ __forceinline__ void operator()(const f32x4 (&acc)[2][2][4][2], const Unit& u, int wr, int wc, int fr, int fq) const {
;     ...
;             for (int g = 0; g < 8; ++g) {
;                 const int ai = g >> 2, m = g & 3, row = rowb + ai * HALF + m * 16; float s = 0.f;
;                 if (g == 2) { EPIRES_LD(6); EPIRES_LD(7); EPI_FENCE(); }
; #pragma unroll
;                 for (int bj = 0; bj < 2; ++bj) {
;                     const f32x4 o0 = bf4_lo(pb[g][bj]) + acc[ai][bj][m][0], o1 = bf4_hi(pb[g][bj]) + acc[ai][bj][m][1];
;                     if (MODE == 2) { float* p = out + (size_t)row * 4096 + colb + 4 * fq + bj * HALF; *(f32x4*)p = o0; *(f32x4*)(p + 16) = o1; }
;                     else { u32x4 w; w.x = pk_bf16(o0[0], o0[1]); w.y = pk_bf16(o0[2], o0[3]); w.z = pk_bf16(o1[0], o1[1]); w.w = pk_bf16(o1[2], o1[3]); *(u32x4*)(hb + blk_elem(row, colb + 8 * fq + bj * HALF, 4096)) = w; s += dot4(o0, o0) + dot4(o1, o1); }
	v_lshlrev_b32_e32 v114, 16, v176
	v_and_b32_e32 v115, 0xffff0000, v176
	v_lshl_add_u64 v[112:113], s[78:79], 0, v[112:113]
	v_lshlrev_b32_e32 v116, 16, v177
	v_and_b32_e32 v117, 0xffff0000, v177
	v_pk_add_f32 v[92:93], v[92:93], v[114:115]
	v_lshlrev_b32_e32 v114, 16, v174
	v_and_b32_e32 v115, 0xffff0000, v174
	v_lshl_add_u64 v[112:113], v[112:113], 0, s[12:13]
	v_pk_add_f32 v[94:95], v[94:95], v[116:117]
	v_lshlrev_b32_e32 v116, 16, v175
	v_and_b32_e32 v117, 0xffff0000, v175
	v_pk_add_f32 v[88:89], v[88:89], v[114:115]
	v_lshl_add_u64 v[112:113], v[112:113], 0, v[130:131]
	v_pk_add_f32 v[90:91], v[90:91], v[116:117]
	global_store_dwordx4 v[112:113], v[92:95], off
	global_store_dwordx4 v[112:113], v[88:91], off offset:64
	v_ashrrev_i32_e32 v163, 31, v162
	v_ashrrev_i32_e32 v147, 31, v146
	v_lshlrev_b32_e32 v88, 16, v170
	v_and_b32_e32 v89, 0xffff0000, v170
	v_lshlrev_b32_e32 v90, 16, v171
	v_and_b32_e32 v91, 0xffff0000, v171
	v_pk_add_f32 v[84:85], v[84:85], v[88:89]
	v_lshlrev_b32_e32 v88, 16, v168
	v_and_b32_e32 v89, 0xffff0000, v168
	v_pk_add_f32 v[86:87], v[86:87], v[90:91]
	v_lshlrev_b32_e32 v90, 16, v169
	v_and_b32_e32 v91, 0xffff0000, v169
	v_pk_add_f32 v[76:77], v[76:77], v[88:89]
	v_pk_add_f32 v[78:79], v[78:79], v[90:91]
	global_store_dwordx4 v[112:113], v[84:87], off offset:512
	global_store_dwordx4 v[112:113], v[76:79], off offset:576
	v_ashrrev_i32_e32 v141, 31, v140
	v_lshlrev_b64 v[84:85], 14, v[162:163]
	v_lshlrev_b32_e32 v76, 16, v166
	v_and_b32_e32 v77, 0xffff0000, v166
	v_pk_add_f32 v[76:77], v[80:81], v[76:77]
	v_lshlrev_b32_e32 v80, 16, v164
	v_and_b32_e32 v81, 0xffff0000, v164
	v_pk_add_f32 v[72:73], v[72:73], v[80:81]
	v_lshl_add_u64 v[80:81], s[78:79], 0, v[84:85]
	v_lshlrev_b32_e32 v78, 16, v167
	v_and_b32_e32 v79, 0xffff0000, v167
	v_lshl_add_u64 v[80:81], v[80:81], 0, s[12:13]
	v_pk_add_f32 v[78:79], v[82:83], v[78:79]
	v_lshlrev_b32_e32 v82, 16, v165
	v_and_b32_e32 v83, 0xffff0000, v165
	v_lshl_add_u64 v[80:81], v[80:81], 0, v[130:131]
	v_pk_add_f32 v[74:75], v[74:75], v[82:83]
	global_store_dwordx4 v[80:81], v[76:79], off
	global_store_dwordx4 v[80:81], v[72:75], off offset:64
	v_ashrrev_i32_e32 v137, 31, v136
	v_ashrrev_i32_e32 v135, 31, v134
	v_lshlrev_b32_e32 v72, 16, v158
	v_and_b32_e32 v73, 0xffff0000, v158
	v_lshlrev_b32_e32 v74, 16, v159
	v_and_b32_e32 v75, 0xffff0000, v159
	v_pk_add_f32 v[68:69], v[68:69], v[72:73]
	v_lshlrev_b32_e32 v72, 16, v154
	v_and_b32_e32 v73, 0xffff0000, v154
	v_pk_add_f32 v[70:71], v[70:71], v[74:75]
	v_lshlrev_b32_e32 v74, 16, v155
	v_and_b32_e32 v75, 0xffff0000, v155
	v_pk_add_f32 v[64:65], v[64:65], v[72:73]
	v_pk_add_f32 v[66:67], v[66:67], v[74:75]
	global_store_dwordx4 v[80:81], v[68:71], off offset:512
	global_store_dwordx4 v[80:81], v[64:67], off offset:576
	s_and_b64 vcc, exec, s[0:1]
	v_lshlrev_b32_e32 v68, 16, v161
	v_lshlrev_b64 v[64:65], 14, v[146:147]
	v_lshlrev_b32_e32 v66, 16, v160
	v_and_b32_e32 v67, 0xffff0000, v160
	v_lshl_add_u64 v[64:65], s[78:79], 0, v[64:65]
	v_and_b32_e32 v69, 0xffff0000, v161
	v_pk_add_f32 v[60:61], v[60:61], v[66:67]
	v_lshlrev_b32_e32 v66, 16, v156
	v_and_b32_e32 v67, 0xffff0000, v156
	v_lshl_add_u64 v[64:65], v[64:65], 0, s[12:13]
	v_pk_add_f32 v[62:63], v[62:63], v[68:69]
	v_lshlrev_b32_e32 v68, 16, v157
	v_and_b32_e32 v69, 0xffff0000, v157
	v_pk_add_f32 v[56:57], v[56:57], v[66:67]
	v_lshl_add_u64 v[64:65], v[64:65], 0, v[130:131]
	v_pk_add_f32 v[58:59], v[58:59], v[68:69]
	global_store_dwordx4 v[64:65], v[60:63], off
	global_store_dwordx4 v[64:65], v[56:59], off offset:64
	s_mov_b64 s[0:1], -1
	s_nop 0
	v_lshlrev_b32_e32 v56, 16, v148
	v_and_b32_e32 v57, 0xffff0000, v148
	v_lshlrev_b32_e32 v58, 16, v149
	v_and_b32_e32 v59, 0xffff0000, v149
	v_pk_add_f32 v[52:53], v[52:53], v[56:57]
	v_lshlrev_b32_e32 v56, 16, v144
	v_and_b32_e32 v57, 0xffff0000, v144
	v_pk_add_f32 v[54:55], v[54:55], v[58:59]
	v_lshlrev_b32_e32 v58, 16, v145
	v_and_b32_e32 v59, 0xffff0000, v145
	v_pk_add_f32 v[44:45], v[44:45], v[56:57]
	v_pk_add_f32 v[46:47], v[46:47], v[58:59]
	global_store_dwordx4 v[64:65], v[52:55], off offset:512
	global_store_dwordx4 v[64:65], v[44:47], off offset:576
	s_nop 0
	v_lshlrev_b64 v[52:53], 14, v[140:141]
	v_lshlrev_b32_e32 v44, 16, v152
	v_and_b32_e32 v45, 0xffff0000, v152
	v_pk_add_f32 v[44:45], v[48:49], v[44:45]
	v_lshlrev_b32_e32 v48, 16, v150
	v_and_b32_e32 v49, 0xffff0000, v150
	v_pk_add_f32 v[40:41], v[40:41], v[48:49]
	v_lshl_add_u64 v[48:49], s[78:79], 0, v[52:53]
	v_lshlrev_b32_e32 v46, 16, v153
	v_and_b32_e32 v47, 0xffff0000, v153
	v_lshl_add_u64 v[48:49], v[48:49], 0, s[12:13]
	v_pk_add_f32 v[46:47], v[50:51], v[46:47]
	v_lshlrev_b32_e32 v50, 16, v151
	v_and_b32_e32 v51, 0xffff0000, v151
	v_lshl_add_u64 v[48:49], v[48:49], 0, v[130:131]
	v_pk_add_f32 v[42:43], v[42:43], v[50:51]
	global_store_dwordx4 v[48:49], v[44:47], off
	global_store_dwordx4 v[48:49], v[40:43], off offset:64
	s_nop 1
	v_lshlrev_b32_e32 v40, 16, v142
	v_and_b32_e32 v41, 0xffff0000, v142
	v_lshlrev_b32_e32 v42, 16, v143
	v_and_b32_e32 v43, 0xffff0000, v143
	v_pk_add_f32 v[36:37], v[36:37], v[40:41]
	v_lshlrev_b32_e32 v40, 16, v138
	v_and_b32_e32 v41, 0xffff0000, v138
	v_pk_add_f32 v[38:39], v[38:39], v[42:43]
	v_lshlrev_b32_e32 v42, 16, v139
	v_and_b32_e32 v43, 0xffff0000, v139
	v_pk_add_f32 v[28:29], v[28:29], v[40:41]
	v_pk_add_f32 v[30:31], v[30:31], v[42:43]
	global_store_dwordx4 v[48:49], v[36:39], off offset:512
	global_store_dwordx4 v[48:49], v[28:31], off offset:576
	s_nop 0
	v_lshlrev_b64 v[36:37], 14, v[136:137]
	s_waitcnt vmcnt(16)
; __device__ __forceinline__ unsigned pk_bf16(float lo, float hi) { const f32x2 f = {lo, hi}; const bf16v2 r = __builtin_convertvector(f, bf16v2); return __builtin_bit_cast(unsigned, r); }
; __device__ __forceinline__ float dot4(const f32x4 a, const f32x4 b) { return (a[0] * b[0] + a[1] * b[1]) + (a[2] * b[2] + a[3] * b[3]); }
; #define EPI_FENCE() asm volatile("" ::: "memory")
; #define PG8_BAR __builtin_amdgcn_s_barrier()
;     __device__ __forceinline__ void operator()(const f32x4 (&acc)[2][2][4][2], const Unit& u, int wr, int wc, int fr, int fq) const {
;     ...
;             for (int g = 0; g < 8; ++g) {
;                 const int ai = g >> 2, m = g & 3, row = rowb + ai * HALF + m * 16; float s = 0.f;
;                 if (g == 2) { EPIRES_LD(6); EPIRES_LD(7); EPI_FENCE(); }
; #pragma unroll
;                 for (int bj = 0; bj < 2; ++bj) {
;                     const f32x4 o0 = bf4_lo(pb[g][bj]) + acc[ai][bj][m][0], o1 = bf4_hi(pb[g][bj]) + acc[ai][bj][m][1];
;                     if (MODE == 2) { float* p = out + (size_t)row * 4096 + colb + 4 * fq + bj * HALF; *(f32x4*)p = o0; *(f32x4*)(p + 16) = o1; }
;                     else { u32x4 w; w.x = pk_bf16(o0[0], o0[1]); w.y = pk_bf16(o0[2], o0[3]); w.z = pk_bf16(o1[0], o1[1]); w.w = pk_bf16(o1[2], o1[3]); *(u32x4*)(hb + blk_elem(row, colb + 8 * fq + bj * HALF, 4096)) = w; s += dot4(o0, o0) + dot4(o1, o1); }
;                 }
;                 if (MODE != 2) { s += __shfl_xor(s, 16); s += __shfl_xor(s, 32); if (fq == 0) __hip_atomic_fetch_add(ssq + row, s, __ATOMIC_RELAXED, __HIP_MEMORY_SCOPE_AGENT); }
;             }
; template <class Epi, class Sched, bool ALIGN_EPI = false, bool SP2 = false, bool HALFM = false>
; __device__ __forceinline__ void gemm_phase(PG8_LAS unsigned char* lds, const Gemm g, const Sched& S, const Epi& E) {
;     ...
;         if (!has_next) break;
; #pragma unroll
;         for (int a = 0; a < 2; ++a)
; #pragma unroll
;             for (int b = 0; b < 2; ++b)
; #pragma unroll
;                 for (int m = 0; m < 4; ++m)
; #pragma unroll
;                     for (int n = 0; n < 2; ++n) acc[a][b][m][n] = (f32x4){0.f, 0.f, 0.f, 0.f};
;         cur = nxt; cA = nA; cB = nB; ++ui;
;         if constexpr (ALIGN_EPI) { if (wr == 1) PG8_BAR; }
	v_lshlrev_b32_e32 v28, 16, v110
	v_and_b32_e32 v29, 0xffff0000, v110
	v_pk_add_f32 v[28:29], v[32:33], v[28:29]
	v_lshlrev_b32_e32 v32, 16, v108
	v_and_b32_e32 v33, 0xffff0000, v108
	v_pk_add_f32 v[24:25], v[24:25], v[32:33]
	v_lshl_add_u64 v[32:33], s[78:79], 0, v[36:37]
	v_lshlrev_b32_e32 v30, 16, v111
	v_and_b32_e32 v31, 0xffff0000, v111
	v_lshl_add_u64 v[32:33], v[32:33], 0, s[12:13]
	v_pk_add_f32 v[30:31], v[34:35], v[30:31]
	v_lshlrev_b32_e32 v34, 16, v109
	v_and_b32_e32 v35, 0xffff0000, v109
	v_lshl_add_u64 v[32:33], v[32:33], 0, v[130:131]
	v_pk_add_f32 v[26:27], v[26:27], v[34:35]
	global_store_dwordx4 v[32:33], v[28:31], off
	global_store_dwordx4 v[32:33], v[24:27], off offset:64
	s_nop 1
	v_lshlrev_b32_e32 v24, 16, v104
	v_and_b32_e32 v25, 0xffff0000, v104
	v_lshlrev_b32_e32 v26, 16, v105
	v_and_b32_e32 v27, 0xffff0000, v105
	v_pk_add_f32 v[20:21], v[20:21], v[24:25]
	v_lshlrev_b32_e32 v24, 16, v100
	v_and_b32_e32 v25, 0xffff0000, v100
	v_pk_add_f32 v[22:23], v[22:23], v[26:27]
	v_lshlrev_b32_e32 v26, 16, v101
	v_and_b32_e32 v27, 0xffff0000, v101
	v_pk_add_f32 v[12:13], v[12:13], v[24:25]
	v_pk_add_f32 v[14:15], v[14:15], v[26:27]
	global_store_dwordx4 v[32:33], v[20:23], off offset:512
	global_store_dwordx4 v[32:33], v[12:15], off offset:576
	s_nop 0
	v_lshlrev_b64 v[20:21], 14, v[134:135]
	v_lshlrev_b32_e32 v12, 16, v106
	v_and_b32_e32 v13, 0xffff0000, v106
	v_pk_add_f32 v[12:13], v[16:17], v[12:13]
	v_lshlrev_b32_e32 v16, 16, v102
	v_and_b32_e32 v17, 0xffff0000, v102
	v_lshlrev_b32_e32 v14, 16, v107
	v_and_b32_e32 v15, 0xffff0000, v107
	v_pk_add_f32 v[8:9], v[8:9], v[16:17]
	v_lshl_add_u64 v[16:17], s[78:79], 0, v[20:21]
	v_pk_add_f32 v[14:15], v[18:19], v[14:15]
	v_lshlrev_b32_e32 v18, 16, v103
	v_and_b32_e32 v19, 0xffff0000, v103
	v_lshl_add_u64 v[16:17], v[16:17], 0, s[12:13]
	v_pk_add_f32 v[10:11], v[10:11], v[18:19]
	v_lshl_add_u64 v[16:17], v[16:17], 0, v[130:131]
	global_store_dwordx4 v[16:17], v[12:15], off
	global_store_dwordx4 v[16:17], v[8:11], off offset:64
	s_nop 1
	v_lshlrev_b32_e32 v8, 16, v98
	v_and_b32_e32 v9, 0xffff0000, v98
	v_lshlrev_b32_e32 v10, 16, v99
	v_and_b32_e32 v11, 0xffff0000, v99
	v_pk_add_f32 v[6:7], v[6:7], v[10:11]
	v_pk_add_f32 v[4:5], v[4:5], v[8:9]
	v_lshlrev_b32_e32 v8, 16, v96
	v_and_b32_e32 v9, 0xffff0000, v96
	v_lshlrev_b32_e32 v10, 16, v97
	v_and_b32_e32 v11, 0xffff0000, v97
	v_pk_add_f32 v[2:3], v[2:3], v[10:11]
	v_pk_add_f32 v[0:1], v[0:1], v[8:9]
	global_store_dwordx4 v[16:17], v[4:7], off offset:512
	global_store_dwordx4 v[16:17], v[0:3], off offset:576
	s_cbranch_vccnz .LBB0_1409
	s_andn2_b64 vcc, exec, s[4:5]
	s_cbranch_vccnz .LBB0_1408
	s_barrier
	s_branch .LBB0_1408
